# baseline (speedup 1.0000x reference)
_Z10scan_pass1PKDF16_S0_PKfS0_S2_S2_PDF16_PfS4_S2_S3_:
	s_load_dwordx16 s[8:23], s[0:1], 0x0
	s_load_dwordx4 s[24:27], s[0:1], 0x40
	s_load_dwordx2 s[28:29], s[0:1], 0x50
	s_mov_b32 s64, 0x3d800000
	s_mov_b32 s65, 0x3fb8aa3b
	s_mov_b32 s66, 0x3f317218
	s_mov_b32 s84, 0x40800000
	s_mov_b32 s86, 0x41800000
	s_lshl_b32 s5, s4, 11
	s_lshl_b32 s6, s3, 5
	s_add_i32 s5, s5, s6
	s_lshl_b32 s6, s4, 6
	s_add_i32 s6, s6, s3
	s_getreg_b32 s7, hwreg(HW_REG_HW_ID, 0, 6)
	s_and_b32 s69, s7, 3
	s_lshl_b32 s69, s69, 3
	s_lshr_b32 s7, s7, 4
	s_or_b32 s7, s7, s69
	s_cmp_eq_u32 s7, 0
	s_cbranch_scc1 .Lstag_p1_done
.Lstag_p1_loop:
	s_sleep 7
	s_sub_u32 s7, s7, 1
	s_cmp_lg_u32 s7, 0
	s_cbranch_scc1 .Lstag_p1_loop

_Z10scan_pass2PKDF16_PKfS2_S0_S2_S0_PDF16_S2_:
	s_load_dwordx16 s[8:23], s[0:1], 0x0
	s_mov_b32 s28, 0x3e800000
	s_mov_b32 s29, 0x3c800000
	s_mov_b32 s30, 0x40800000
	s_lshl_b32 s5, s4, 11
	s_lshl_b32 s6, s3, 5
	s_add_i32 s5, s5, s6
	s_lshl_b32 s6, s4, 6
	s_add_i32 s6, s6, s3
	s_getreg_b32 s7, hwreg(HW_REG_HW_ID, 0, 6)
	s_and_b32 s31, s7, 3
	s_lshl_b32 s31, s31, 3
	s_lshr_b32 s7, s7, 4
	s_or_b32 s7, s7, s31
	s_cmp_eq_u32 s7, 0
	s_cbranch_scc1 .Lstag_p2_done
